# baseline (speedup 1.0000x reference)
_Z7gemm_dbILi256ELi192ELi64ELi96ELi64ELi2ELi1ELi4EEvPKDF16_S1_PfPDF16_S3_S3_PK15HIP_vector_typeIfLj2EEiii:
	s_load_dwordx4 s[4:7], s[0:1], 0x38
	s_waitcnt lgkmcnt(0)
	s_and_b32 s7, s2, 7
	s_lshr_b32 s2, s2, 3
	v_readfirstlane_b32 s14, v0
	s_mul_hi_i32 s3, s5, 0x2aaaaaab
	s_lshr_b32 s5, s3, 31
	s_ashr_i32 s3, s3, 5
	s_add_i32 s3, s3, s5
	s_abs_i32 s5, s3
	v_cvt_f32_u32_e32 v1, s5
	s_ashr_i32 s8, s4, 31
	s_lshr_b32 s8, s8, 21
	s_add_i32 s4, s4, s8
	v_rcp_iflag_f32_e32 v1, v1
	s_ashr_i32 s4, s4, 11
	s_mul_i32 s4, s4, s7
	s_sub_i32 s7, 0, s5
	v_mul_f32_e32 v1, 0x4f7ffffe, v1
	v_cvt_u32_f32_e32 v1, v1
	s_ashr_i32 s8, s3, 31
	v_readfirstlane_b32 s9, v1
	s_mul_i32 s7, s7, s9
	s_mul_hi_u32 s7, s9, s7
	s_add_i32 s9, s9, s7
	s_mul_hi_u32 s7, s2, s9
	s_mul_i32 s9, s7, s5
	s_sub_i32 s9, s2, s9
	s_add_i32 s10, s7, 1
	s_sub_i32 s11, s9, s5
	s_cmp_ge_u32 s9, s5
	s_cselect_b32 s7, s10, s7
	s_cselect_b32 s9, s11, s9
	s_add_i32 s10, s7, 1
	s_cmp_ge_u32 s9, s5
	s_cselect_b32 s5, s10, s7
	s_xor_b32 s5, s5, s8
	s_sub_i32 s5, s5, s8
	s_add_i32 s4, s5, s4
	s_mul_i32 s5, s5, s3
	s_sub_i32 s15, s2, s5
	s_ashr_i32 s2, s6, 31
	s_lshr_b32 s2, s2, 26
	s_add_i32 s2, s6, s2
	s_lshl_b32 s12, s4, 8
	s_ashr_i32 s7, s2, 6
	s_cmpk_lt_u32 s14, 0x200
	s_cselect_b64 s[2:3], -1, 0
	s_mul_i32 s13, s15, 0xc0
	s_mov_b64 s[4:5], -1
	s_and_b64 vcc, exec, s[2:3]
	s_cbranch_vccnz .LBB2_9
	v_add_u32_e32 v1, 0xfffffe00, v0
	s_load_dwordx4 s[8:11], s[0:1], 0x0
	v_lshlrev_b32_e32 v18, 4, v1
	v_ashrrev_i32_e32 v19, 3, v1
	v_lshrrev_b32_e32 v1, 4, v1
	v_xor_b32_e32 v1, v1, v0
	v_lshlrev_b32_e32 v1, 4, v1
	v_and_b32_e32 v28, 0x70, v1
	v_add_u32_e32 v1, 0, v18
	v_add_u32_e32 v4, 0x1000, v18
	v_add_u32_e32 v6, 0x2000, v18
	v_add_u32_e32 v8, 0x3000, v18
	v_add_u32_e32 v10, 0x4000, v18
	v_add_u32_e32 v12, 0x5000, v18
	v_add_u32_e32 v14, 0x6000, v18
	v_add_u32_e32 v18, 0x7000, v18
	v_ashrrev_i32_e32 v20, 7, v4
	v_lshrrev_b32_e32 v22, 7, v6
	v_lshrrev_b32_e32 v24, 7, v8
	v_lshrrev_b32_e32 v26, 7, v10
	v_lshrrev_b32_e32 v36, 7, v12
	v_lshrrev_b32_e32 v14, 7, v14
	v_lshrrev_b32_e32 v18, 7, v18
	v_add_u32_e32 v2, s12, v19
	s_movk_i32 s16, 0x880
	s_waitcnt lgkmcnt(0)
	v_mov_b64_e32 v[16:17], s[8:9]
	v_add_u32_e32 v4, s12, v20
	v_add_u32_e32 v6, s12, v22
	v_add_u32_e32 v8, s12, v24
	v_add_u32_e32 v10, s12, v26
	v_add_u32_e32 v12, s12, v36
	v_add_u32_e32 v14, s12, v14
	v_add_u32_e32 v18, s12, v18
	v_mad_i64_i32 v[2:3], s[4:5], v2, s16, v[16:17]
	v_mad_i64_i32 v[4:5], s[4:5], v4, s16, v[16:17]
	v_mad_i64_i32 v[6:7], s[4:5], v6, s16, v[16:17]
	v_mad_i64_i32 v[8:9], s[4:5], v8, s16, v[16:17]
	v_mad_i64_i32 v[10:11], s[4:5], v10, s16, v[16:17]
	v_mad_i64_i32 v[12:13], s[4:5], v12, s16, v[16:17]
	v_mad_i64_i32 v[14:15], s[4:5], v14, s16, v[16:17]
	v_mad_i64_i32 v[16:17], s[4:5], v18, s16, v[16:17]
	v_add_u32_e32 v18, s13, v19
	v_mov_b64_e32 v[30:31], s[10:11]
	v_add_u32_e32 v20, s13, v20
	v_add_u32_e32 v22, s13, v22
	v_add_u32_e32 v24, s13, v24
	v_add_u32_e32 v26, s13, v26
	v_add_u32_e32 v36, s13, v36
	v_mad_i64_i32 v[18:19], s[4:5], v18, s16, v[30:31]
	v_mad_i64_i32 v[20:21], s[4:5], v20, s16, v[30:31]
	v_mad_u64_u32 v[22:23], s[4:5], v22, s16, v[30:31]
	v_mad_u64_u32 v[24:25], s[4:5], v24, s16, v[30:31]
	v_mad_u64_u32 v[26:27], s[4:5], v26, s16, v[30:31]
	v_mad_u64_u32 v[30:31], s[4:5], v36, s16, v[30:31]
	v_mov_b32_e32 v29, 0
	v_add_u32_e32 v32, 0x1000, v1
	v_readfirstlane_b32 s4, v1
	v_lshl_add_u64 v[2:3], v[2:3], 0, v[28:29]
	v_add_u32_e32 v33, 0x2000, v1
	s_mov_b32 m0, s4
	v_readfirstlane_b32 s4, v32
	v_lshl_add_u64 v[4:5], v[4:5], 0, v[28:29]
	v_add_u32_e32 v34, 0x3000, v1
	global_load_lds_dwordx4 v[2:3], off
	s_mov_b32 m0, s4
	v_readfirstlane_b32 s4, v33
	v_lshl_add_u64 v[6:7], v[6:7], 0, v[28:29]
	v_add_u32_e32 v35, 0x4000, v1
	global_load_lds_dwordx4 v[4:5], off
	s_mov_b32 m0, s4
	v_readfirstlane_b32 s4, v34
	v_lshl_add_u64 v[8:9], v[8:9], 0, v[28:29]
	v_add_u32_e32 v37, 0x5000, v1
	global_load_lds_dwordx4 v[6:7], off
	s_mov_b32 m0, s4
	v_readfirstlane_b32 s4, v35
	v_lshl_add_u64 v[10:11], v[10:11], 0, v[28:29]
	v_add_u32_e32 v38, 0x6000, v1
	global_load_lds_dwordx4 v[8:9], off
	s_mov_b32 m0, s4
	v_readfirstlane_b32 s4, v37
	v_lshl_add_u64 v[12:13], v[12:13], 0, v[28:29]
	v_add_u32_e32 v39, 0x7000, v1
	global_load_lds_dwordx4 v[10:11], off
	s_mov_b32 m0, s4
	v_readfirstlane_b32 s4, v38
	v_lshl_add_u64 v[14:15], v[14:15], 0, v[28:29]
	v_add_u32_e32 v40, 0x18000, v1
	global_load_lds_dwordx4 v[12:13], off
	s_mov_b32 m0, s4
	v_readfirstlane_b32 s4, v39
	v_lshl_add_u64 v[16:17], v[16:17], 0, v[28:29]
	v_add_u32_e32 v41, 0x19000, v1
	global_load_lds_dwordx4 v[14:15], off
	s_mov_b32 m0, s4
	v_readfirstlane_b32 s4, v40
	v_lshl_add_u64 v[18:19], v[18:19], 0, v[28:29]
	v_add_u32_e32 v42, 0x1a000, v1
	global_load_lds_dwordx4 v[16:17], off
	s_mov_b32 m0, s4
	v_readfirstlane_b32 s4, v41
	v_lshl_add_u64 v[20:21], v[20:21], 0, v[28:29]
	v_add_u32_e32 v43, 0x1b000, v1
	global_load_lds_dwordx4 v[18:19], off
	s_mov_b32 m0, s4
	v_readfirstlane_b32 s4, v42
	v_lshl_add_u64 v[22:23], v[22:23], 0, v[28:29]
	v_add_u32_e32 v44, 0x1c000, v1
	global_load_lds_dwordx4 v[20:21], off
	s_mov_b32 m0, s4
	v_readfirstlane_b32 s4, v43
	v_lshl_add_u64 v[24:25], v[24:25], 0, v[28:29]
	v_lshl_add_u64 v[26:27], v[26:27], 0, v[28:29]
	v_lshl_add_u64 v[28:29], v[30:31], 0, v[28:29]
	v_add_u32_e32 v30, 0x1d000, v1
	global_load_lds_dwordx4 v[22:23], off
	s_mov_b32 m0, s4
	v_readfirstlane_b32 s4, v44
	global_load_lds_dwordx4 v[24:25], off
	s_mov_b32 m0, s4
	v_readfirstlane_b32 s4, v30
	global_load_lds_dwordx4 v[26:27], off
	s_mov_b32 m0, s4
	s_cmp_lt_i32 s6, 64
	global_load_lds_dwordx4 v[28:29], off
	v_readfirstlane_b32 s18, v1
	s_movk_i32 s8, 0x80
	s_mov_b32 s9, 0
	s_add_i32 s17, s18, 0x8000
	s_mov_b32 m0, s17
	v_lshl_add_u64 v[30:31], v[2:3], 0, s[8:9]
	s_add_i32 s17, s17, 0x1000
	global_load_lds_dwordx4 v[30:31], off
	s_mov_b32 m0, s17
	v_lshl_add_u64 v[30:31], v[4:5], 0, s[8:9]
	s_add_i32 s17, s17, 0x1000
	global_load_lds_dwordx4 v[30:31], off
	s_mov_b32 m0, s17
	v_lshl_add_u64 v[30:31], v[6:7], 0, s[8:9]
	s_add_i32 s17, s17, 0x1000
	global_load_lds_dwordx4 v[30:31], off
	s_mov_b32 m0, s17
	v_lshl_add_u64 v[30:31], v[8:9], 0, s[8:9]
	s_add_i32 s17, s17, 0x1000
	global_load_lds_dwordx4 v[30:31], off
	s_mov_b32 m0, s17
	v_lshl_add_u64 v[30:31], v[10:11], 0, s[8:9]
	s_add_i32 s17, s17, 0x1000
	global_load_lds_dwordx4 v[30:31], off
	s_mov_b32 m0, s17
	v_lshl_add_u64 v[30:31], v[12:13], 0, s[8:9]
	s_add_i32 s17, s17, 0x1000
	global_load_lds_dwordx4 v[30:31], off
	s_mov_b32 m0, s17
	v_lshl_add_u64 v[30:31], v[14:15], 0, s[8:9]
	s_add_i32 s17, s17, 0x1000
	global_load_lds_dwordx4 v[30:31], off
	s_mov_b32 m0, s17
	v_lshl_add_u64 v[30:31], v[16:17], 0, s[8:9]
	s_add_i32 s17, s17, 0x1000
	global_load_lds_dwordx4 v[30:31], off
	s_waitcnt vmcnt(8)
	s_barrier
	s_mov_b32 s11, 0
	s_mov_b32 s19, 0x10000
.Lq_ld_loop:
	s_add_i32 s16, s11, 1
	s_cmp_ge_i32 s16, s7
	s_cbranch_scc1 .Lq_ld_nomore
	s_lshl_b32 s8, s16, 7
	s_mov_b32 s9, 0
	s_and_b32 s17, s16, 1
	s_mul_i32 s17, s17, 0x6000
	s_add_i32 s17, s17, s18
	s_add_i32 s17, s17, 0x18000
	s_mov_b32 m0, s17
	v_lshl_add_u64 v[30:31], v[18:19], 0, s[8:9]
	s_add_i32 s17, s17, 0x1000
	global_load_lds_dwordx4 v[30:31], off
	s_mov_b32 m0, s17
	v_lshl_add_u64 v[30:31], v[20:21], 0, s[8:9]
	s_add_i32 s17, s17, 0x1000
	global_load_lds_dwordx4 v[30:31], off
	s_mov_b32 m0, s17
	v_lshl_add_u64 v[30:31], v[22:23], 0, s[8:9]
	s_add_i32 s17, s17, 0x1000
	global_load_lds_dwordx4 v[30:31], off
	s_mov_b32 m0, s17
	v_lshl_add_u64 v[30:31], v[24:25], 0, s[8:9]
	s_add_i32 s17, s17, 0x1000
	global_load_lds_dwordx4 v[30:31], off
	s_mov_b32 m0, s17
	v_lshl_add_u64 v[30:31], v[26:27], 0, s[8:9]
	s_add_i32 s17, s17, 0x1000
	global_load_lds_dwordx4 v[30:31], off
	s_mov_b32 m0, s17
	v_lshl_add_u64 v[30:31], v[28:29], 0, s[8:9]
	s_add_i32 s17, s17, 0x1000
	global_load_lds_dwordx4 v[30:31], off
	s_add_i32 s16, s11, 2
	s_cmp_ge_i32 s16, s7
	s_cbranch_scc1 .Lq_ld_lastb
	s_lshl_b32 s8, s16, 7
	s_add_i32 s17, s19, s18
	s_mov_b32 m0, s17
	v_lshl_add_u64 v[30:31], v[2:3], 0, s[8:9]
	s_add_i32 s17, s17, 0x1000
	global_load_lds_dwordx4 v[30:31], off
	s_mov_b32 m0, s17
	v_lshl_add_u64 v[30:31], v[4:5], 0, s[8:9]
	s_add_i32 s17, s17, 0x1000
	global_load_lds_dwordx4 v[30:31], off
	s_mov_b32 m0, s17
	v_lshl_add_u64 v[30:31], v[6:7], 0, s[8:9]
	s_add_i32 s17, s17, 0x1000
	global_load_lds_dwordx4 v[30:31], off
	s_mov_b32 m0, s17
	v_lshl_add_u64 v[30:31], v[8:9], 0, s[8:9]
	s_add_i32 s17, s17, 0x1000
	global_load_lds_dwordx4 v[30:31], off
	s_mov_b32 m0, s17
	v_lshl_add_u64 v[30:31], v[10:11], 0, s[8:9]
	s_add_i32 s17, s17, 0x1000
	global_load_lds_dwordx4 v[30:31], off
	s_mov_b32 m0, s17
	v_lshl_add_u64 v[30:31], v[12:13], 0, s[8:9]
	s_add_i32 s17, s17, 0x1000
	global_load_lds_dwordx4 v[30:31], off
	s_mov_b32 m0, s17
	v_lshl_add_u64 v[30:31], v[14:15], 0, s[8:9]
	s_add_i32 s17, s17, 0x1000
	global_load_lds_dwordx4 v[30:31], off
	s_mov_b32 m0, s17
	v_lshl_add_u64 v[30:31], v[16:17], 0, s[8:9]
	s_add_i32 s17, s17, 0x1000
	global_load_lds_dwordx4 v[30:31], off
	s_add_i32 s19, s19, 0x8000
	s_cmp_lg_u32 s19, 0x18000
	s_cselect_b32 s19, s19, 0
	s_waitcnt vmcnt(8)
	s_barrier
	s_add_i32 s11, s11, 1
	s_branch .Lq_ld_loop
.Lq_ld_lastb:
	s_waitcnt vmcnt(0)
	s_barrier
	s_add_i32 s11, s11, 1
	s_branch .Lq_ld_loop
.Lq_ld_nomore:
	s_waitcnt vmcnt(0)
	s_barrier

.LBB2_9:
	s_lshr_b32 s8, s14, 7
	v_and_b32_e32 v1, 15, v0
	v_bfe_u32 v98, v0, 4, 2
	s_bfe_u32 s9, s14, 0x10006
	s_and_b64 vcc, exec, s[4:5]
	s_cbranch_vccz .LBB2_13
	s_barrier
	s_cmp_lt_i32 s6, 64
	s_mov_b32 s4, 0
	s_cbranch_scc1 .LBB2_41
	v_lshrrev_b32_e32 v2, 1, v0
	v_bfe_u32 v3, v0, 1, 3
	v_bitop3_b32 v2, v98, v2, 7 bitop3:0x78
	s_mul_i32 s5, s9, 0x60
	v_lshlrev_b32_e32 v99, 4, v2
	v_bitop3_b32 v2, v98, v3, 4 bitop3:0x36
	v_or_b32_e32 v4, s5, v1
	v_lshlrev_b32_e32 v102, 4, v2
	v_mov_b32_e32 v2, 0
	s_lshl_b32 s5, s8, 13
	v_lshlrev_b32_e32 v100, 7, v1
	v_lshlrev_b32_e32 v101, 7, v4
	v_mov_b32_e32 v3, v2
	v_mov_b32_e32 v4, v2
	v_mov_b32_e32 v5, v2
	v_mov_b32_e32 v6, v2
	v_mov_b32_e32 v7, v2
	v_mov_b32_e32 v8, v2
	v_mov_b32_e32 v9, v2
	v_mov_b32_e32 v34, v2
	v_mov_b32_e32 v35, v2
	v_mov_b32_e32 v36, v2
	v_mov_b32_e32 v37, v2
	v_mov_b32_e32 v38, v2
	v_mov_b32_e32 v39, v2
	v_mov_b32_e32 v40, v2
	v_mov_b32_e32 v41, v2
	v_mov_b32_e32 v66, v2
	v_mov_b32_e32 v67, v2
	v_mov_b32_e32 v68, v2
	v_mov_b32_e32 v69, v2
	v_mov_b32_e32 v70, v2
	v_mov_b32_e32 v71, v2
	v_mov_b32_e32 v72, v2
	v_mov_b32_e32 v73, v2
	v_mov_b32_e32 v10, v2
	v_mov_b32_e32 v11, v2
	v_mov_b32_e32 v12, v2
	v_mov_b32_e32 v13, v2
	v_mov_b32_e32 v14, v2
	v_mov_b32_e32 v15, v2
	v_mov_b32_e32 v16, v2
	v_mov_b32_e32 v17, v2
	v_mov_b32_e32 v42, v2
	v_mov_b32_e32 v43, v2
	v_mov_b32_e32 v44, v2
	v_mov_b32_e32 v45, v2
	v_mov_b32_e32 v46, v2
	v_mov_b32_e32 v47, v2
	v_mov_b32_e32 v48, v2
	v_mov_b32_e32 v49, v2
	v_mov_b32_e32 v74, v2
	v_mov_b32_e32 v75, v2
	v_mov_b32_e32 v76, v2
	v_mov_b32_e32 v77, v2
	v_mov_b32_e32 v78, v2
	v_mov_b32_e32 v79, v2
	v_mov_b32_e32 v80, v2
	v_mov_b32_e32 v81, v2
	v_mov_b32_e32 v18, v2
	v_mov_b32_e32 v19, v2
	v_mov_b32_e32 v20, v2
	v_mov_b32_e32 v21, v2
	v_mov_b32_e32 v22, v2
	v_mov_b32_e32 v23, v2
	v_mov_b32_e32 v24, v2
	v_mov_b32_e32 v25, v2
	v_mov_b32_e32 v50, v2
	v_mov_b32_e32 v51, v2
	v_mov_b32_e32 v52, v2
	v_mov_b32_e32 v53, v2
	v_mov_b32_e32 v54, v2
	v_mov_b32_e32 v55, v2
	v_mov_b32_e32 v56, v2
	v_mov_b32_e32 v57, v2
	v_mov_b32_e32 v82, v2
	v_mov_b32_e32 v83, v2
	v_mov_b32_e32 v84, v2
	v_mov_b32_e32 v85, v2
	v_mov_b32_e32 v86, v2
	v_mov_b32_e32 v87, v2
	v_mov_b32_e32 v88, v2
	v_mov_b32_e32 v89, v2
	v_mov_b32_e32 v26, v2
	v_mov_b32_e32 v27, v2
	v_mov_b32_e32 v28, v2
	v_mov_b32_e32 v29, v2
	v_mov_b32_e32 v30, v2
	v_mov_b32_e32 v31, v2
	v_mov_b32_e32 v32, v2
	v_mov_b32_e32 v33, v2
	v_mov_b32_e32 v58, v2
	v_mov_b32_e32 v59, v2
	v_mov_b32_e32 v60, v2
	v_mov_b32_e32 v61, v2
	v_mov_b32_e32 v62, v2
	v_mov_b32_e32 v63, v2
	v_mov_b32_e32 v64, v2
	v_mov_b32_e32 v65, v2
	v_mov_b32_e32 v90, v2
	v_mov_b32_e32 v91, v2
	v_mov_b32_e32 v92, v2
	v_mov_b32_e32 v93, v2
	v_mov_b32_e32 v94, v2
	v_mov_b32_e32 v95, v2
	v_mov_b32_e32 v96, v2
	v_mov_b32_e32 v97, v2
	s_mov_b32 s20, 0
.LBB2_12:
	s_mul_i32 s6, s4, 0x6000
	s_add_i32 s6, s6, 0x10000
	v_add_u32_e32 v136, s20, v99
	v_add3_u32 v136, v136, s5, v100
	v_add_u32_e32 v103, s6, v99
	v_add_u32_e32 v103, v103, v101
	ds_read_b128 v[104:107], v103 offset:32768
	ds_read_b128 v[108:111], v103 offset:34816
	ds_read_b128 v[112:115], v136
	ds_read_b128 v[116:119], v136 offset:2048
	ds_read_b128 v[120:123], v103 offset:36864
	ds_read_b128 v[124:127], v103 offset:38912
	ds_read_b128 v[128:131], v103 offset:40960
	ds_read_b128 v[132:135], v103 offset:43008
	s_waitcnt lgkmcnt(0)
	v_mfma_f32_16x16x32_f16 v[94:97], v[104:107], v[112:115], v[94:97]
	v_add_u32_e32 v103, s6, v102
	v_mfma_f32_16x16x32_f16 v[90:93], v[108:111], v[112:115], v[90:93]
	v_mfma_f32_16x16x32_f16 v[62:65], v[120:123], v[112:115], v[62:65]
	v_mfma_f32_16x16x32_f16 v[58:61], v[124:127], v[112:115], v[58:61]
	v_mfma_f32_16x16x32_f16 v[30:33], v[128:131], v[112:115], v[30:33]
	v_mfma_f32_16x16x32_f16 v[26:29], v[132:135], v[112:115], v[26:29]
	v_mfma_f32_16x16x32_f16 v[86:89], v[104:107], v[116:119], v[86:89]
	v_mfma_f32_16x16x32_f16 v[82:85], v[108:111], v[116:119], v[82:85]
	v_mfma_f32_16x16x32_f16 v[54:57], v[120:123], v[116:119], v[54:57]
	v_mfma_f32_16x16x32_f16 v[50:53], v[124:127], v[116:119], v[50:53]
	v_mfma_f32_16x16x32_f16 v[22:25], v[128:131], v[116:119], v[22:25]
	v_mfma_f32_16x16x32_f16 v[18:21], v[132:135], v[116:119], v[18:21]
	ds_read_b128 v[112:115], v136 offset:4096
	ds_read_b128 v[116:119], v136 offset:6144
	v_add_u32_e32 v136, s20, v102
	v_add3_u32 v136, v136, s5, v100
	v_add_u32_e32 v103, v103, v101
	s_waitcnt lgkmcnt(0)
	v_mfma_f32_16x16x32_f16 v[78:81], v[104:107], v[112:115], v[78:81]
	v_mfma_f32_16x16x32_f16 v[74:77], v[108:111], v[112:115], v[74:77]
	v_mfma_f32_16x16x32_f16 v[46:49], v[120:123], v[112:115], v[46:49]
	v_mfma_f32_16x16x32_f16 v[42:45], v[124:127], v[112:115], v[42:45]
	v_mfma_f32_16x16x32_f16 v[14:17], v[128:131], v[112:115], v[14:17]
	v_mfma_f32_16x16x32_f16 v[10:13], v[132:135], v[112:115], v[10:13]
	v_mfma_f32_16x16x32_f16 v[70:73], v[104:107], v[116:119], v[70:73]
	v_mfma_f32_16x16x32_f16 v[66:69], v[108:111], v[116:119], v[66:69]
	ds_read_b128 v[104:107], v103 offset:32768
	ds_read_b128 v[108:111], v103 offset:34816
	v_mfma_f32_16x16x32_f16 v[38:41], v[120:123], v[116:119], v[38:41]
	v_mfma_f32_16x16x32_f16 v[34:37], v[124:127], v[116:119], v[34:37]
	v_mfma_f32_16x16x32_f16 v[6:9], v[128:131], v[116:119], v[6:9]
	v_mfma_f32_16x16x32_f16 v[2:5], v[132:135], v[116:119], v[2:5]
	ds_read_b128 v[112:115], v136
	ds_read_b128 v[116:119], v136 offset:2048
	ds_read_b128 v[120:123], v103 offset:36864
	ds_read_b128 v[124:127], v103 offset:38912
	ds_read_b128 v[128:131], v103 offset:40960
	ds_read_b128 v[132:135], v103 offset:43008
	s_waitcnt lgkmcnt(0)
	v_mfma_f32_16x16x32_f16 v[94:97], v[104:107], v[112:115], v[94:97]
	v_mfma_f32_16x16x32_f16 v[90:93], v[108:111], v[112:115], v[90:93]
	v_mfma_f32_16x16x32_f16 v[62:65], v[120:123], v[112:115], v[62:65]
	v_mfma_f32_16x16x32_f16 v[58:61], v[124:127], v[112:115], v[58:61]
	v_mfma_f32_16x16x32_f16 v[30:33], v[128:131], v[112:115], v[30:33]
	v_mfma_f32_16x16x32_f16 v[26:29], v[132:135], v[112:115], v[26:29]
	v_mfma_f32_16x16x32_f16 v[86:89], v[104:107], v[116:119], v[86:89]
	v_mfma_f32_16x16x32_f16 v[82:85], v[108:111], v[116:119], v[82:85]
	v_mfma_f32_16x16x32_f16 v[54:57], v[120:123], v[116:119], v[54:57]
	v_mfma_f32_16x16x32_f16 v[50:53], v[124:127], v[116:119], v[50:53]
	v_mfma_f32_16x16x32_f16 v[22:25], v[128:131], v[116:119], v[22:25]
	v_mfma_f32_16x16x32_f16 v[18:21], v[132:135], v[116:119], v[18:21]
	ds_read_b128 v[112:115], v136 offset:4096
	ds_read_b128 v[116:119], v136 offset:6144
	s_waitcnt lgkmcnt(0)
	s_barrier
	s_waitcnt lgkmcnt(0)
	v_mfma_f32_16x16x32_f16 v[78:81], v[104:107], v[112:115], v[78:81]
	v_mfma_f32_16x16x32_f16 v[74:77], v[108:111], v[112:115], v[74:77]
	v_mfma_f32_16x16x32_f16 v[46:49], v[120:123], v[112:115], v[46:49]
	v_mfma_f32_16x16x32_f16 v[42:45], v[124:127], v[112:115], v[42:45]
	v_mfma_f32_16x16x32_f16 v[14:17], v[128:131], v[112:115], v[14:17]
	v_mfma_f32_16x16x32_f16 v[10:13], v[132:135], v[112:115], v[10:13]
	v_mfma_f32_16x16x32_f16 v[70:73], v[104:107], v[116:119], v[70:73]
	v_mfma_f32_16x16x32_f16 v[66:69], v[108:111], v[116:119], v[66:69]
	v_mfma_f32_16x16x32_f16 v[38:41], v[120:123], v[116:119], v[38:41]
	v_mfma_f32_16x16x32_f16 v[34:37], v[124:127], v[116:119], v[34:37]
	v_mfma_f32_16x16x32_f16 v[6:9], v[128:131], v[116:119], v[6:9]
	v_mfma_f32_16x16x32_f16 v[2:5], v[132:135], v[116:119], v[2:5]
	s_add_i32 s4, s4, 1
	s_cmp_lg_u32 s4, 2
	s_cselect_b32 s4, s4, 0
	s_add_i32 s20, s20, 0x8000
	s_cmp_lg_u32 s20, 0x18000
	s_cselect_b32 s20, s20, 0
	s_add_i32 s7, s7, -1
	s_cmp_lg_u32 s7, 0
	s_cbranch_scc1 .LBB2_12
	s_branch .LBB2_14

	.amdhsa_kernel _Z7gemm_dbILi256ELi192ELi64ELi96ELi64ELi2ELi1ELi4EEvPKDF16_S1_PfPDF16_S3_S3_PK15HIP_vector_typeIfLj2EEiii
		.amdhsa_group_segment_fixed_size 32768
		.amdhsa_private_segment_fixed_size 0
		.amdhsa_kernarg_size 68
		.amdhsa_user_sgpr_count 2
		.amdhsa_user_sgpr_dispatch_ptr 0
		.amdhsa_user_sgpr_queue_ptr 0
		.amdhsa_user_sgpr_kernarg_segment_ptr 1
		.amdhsa_user_sgpr_dispatch_id 0
		.amdhsa_user_sgpr_kernarg_preload_length 0
		.amdhsa_user_sgpr_kernarg_preload_offset 0
		.amdhsa_user_sgpr_private_segment_size 0
		.amdhsa_uses_dynamic_stack 0
		.amdhsa_enable_private_segment 0
		.amdhsa_system_sgpr_workgroup_id_x 1
		.amdhsa_system_sgpr_workgroup_id_y 0
		.amdhsa_system_sgpr_workgroup_id_z 0
		.amdhsa_system_sgpr_workgroup_info 0
		.amdhsa_system_vgpr_workitem_id 0
		.amdhsa_next_free_vgpr 137
		.amdhsa_next_free_sgpr 21
		.amdhsa_accum_offset 140
		.amdhsa_reserve_vcc 1
		.amdhsa_float_round_mode_32 0
		.amdhsa_float_round_mode_16_64 0
		.amdhsa_float_denorm_mode_32 3
		.amdhsa_float_denorm_mode_16_64 3
		.amdhsa_dx10_clamp 1
		.amdhsa_ieee_mode 1
		.amdhsa_fp16_overflow 0
		.amdhsa_tg_split 0
		.amdhsa_exception_fp_ieee_invalid_op 0
		.amdhsa_exception_fp_denorm_src 0
		.amdhsa_exception_fp_ieee_div_zero 0
		.amdhsa_exception_fp_ieee_overflow 0
		.amdhsa_exception_fp_ieee_underflow 0
		.amdhsa_exception_fp_ieee_inexact 0
		.amdhsa_exception_int_div_zero 0
	.end_amdhsa_kernel

amdhsa.kernels:
  - .agpr_count:     0
    .args:
      - .actual_access:  read_only
        .address_space:  global
        .offset:         0
        .size:           8
        .value_kind:     global_buffer
      - .actual_access:  read_only
        .address_space:  global
        .offset:         8
        .size:           8
        .value_kind:     global_buffer
      - .actual_access:  read_only
        .address_space:  global
        .offset:         16
        .size:           8
        .value_kind:     global_buffer
      - .actual_access:  read_only
        .address_space:  global
        .offset:         24
        .size:           8
        .value_kind:     global_buffer
      - .actual_access:  read_only
        .address_space:  global
        .offset:         32
        .size:           8
        .value_kind:     global_buffer
      - .address_space:  global
        .offset:         40
        .size:           8
        .value_kind:     global_buffer
      - .address_space:  global
        .offset:         48
        .size:           8
        .value_kind:     global_buffer
      - .address_space:  global
        .offset:         56
        .size:           8
        .value_kind:     global_buffer
      - .address_space:  global
        .offset:         64
        .size:           8
        .value_kind:     global_buffer
    .group_segment_fixed_size: 0
    .kernarg_segment_align: 8
    .kernarg_segment_size: 72
    .language:       OpenCL C
    .language_version:
      - 2
      - 0
    .max_flat_workgroup_size: 256
    .name:           _Z11prep_kernelPKfS0_S0_S0_S0_PDF16_S1_S1_P15HIP_vector_typeIfLj2EE
    .private_segment_fixed_size: 0
    .sgpr_count:     22
    .sgpr_spill_count: 0
    .symbol:         _Z11prep_kernelPKfS0_S0_S0_S0_PDF16_S1_S1_P15HIP_vector_typeIfLj2EE.kd
    .uniform_work_group_size: 1
    .uses_dynamic_stack: false
    .vgpr_count:     20
    .vgpr_spill_count: 0
    .wavefront_size: 64
  - .agpr_count:     0
    .args:
      - .address_space:  global
        .offset:         0
        .size:           8
        .value_kind:     global_buffer
      - .address_space:  global
        .offset:         8
        .size:           8
        .value_kind:     global_buffer
      - .address_space:  global
        .offset:         16
        .size:           8
        .value_kind:     global_buffer
      - .address_space:  global
        .offset:         24
        .size:           8
        .value_kind:     global_buffer
    .group_segment_fixed_size: 0
    .kernarg_segment_align: 8
    .kernarg_segment_size: 32
    .language:       OpenCL C
    .language_version:
      - 2
      - 0
    .max_flat_workgroup_size: 512
    .name:           _Z10attn64_fwdPKDF16_S0_S0_PDF16_
    .private_segment_fixed_size: 0
    .sgpr_count:     48
    .sgpr_spill_count: 0
    .symbol:         _Z10attn64_fwdPKDF16_S0_S0_PDF16_.kd
    .uniform_work_group_size: 1
    .uses_dynamic_stack: false
    .vgpr_count:     252
    .vgpr_spill_count: 0
    .wavefront_size: 64
  - .agpr_count:     0
    .args:
      - .address_space:  global
        .offset:         0
        .size:           8
        .value_kind:     global_buffer
      - .address_space:  global
        .offset:         8
        .size:           8
        .value_kind:     global_buffer
      - .address_space:  global
        .offset:         16
        .size:           8
        .value_kind:     global_buffer
      - .address_space:  global
        .offset:         24
        .size:           8
        .value_kind:     global_buffer
      - .address_space:  global
        .offset:         32
        .size:           8
        .value_kind:     global_buffer
      - .address_space:  global
        .offset:         40
        .size:           8
        .value_kind:     global_buffer
      - .actual_access:  read_only
        .address_space:  global
        .offset:         48
        .size:           8
        .value_kind:     global_buffer
      - .offset:         56
        .size:           4
        .value_kind:     by_value
      - .offset:         60
        .size:           4
        .value_kind:     by_value
      - .offset:         64
        .size:           4
        .value_kind:     by_value
    .group_segment_fixed_size: 32768
    .kernarg_segment_align: 8
    .kernarg_segment_size: 68
    .language:       OpenCL C
    .language_version:
      - 2
      - 0
    .max_flat_workgroup_size: 768
    .name:           _Z7gemm_dbILi256ELi192ELi64ELi96ELi64ELi2ELi1ELi4EEvPKDF16_S1_PfPDF16_S3_S3_PK15HIP_vector_typeIfLj2EEiii
    .private_segment_fixed_size: 0
    .sgpr_count:     27
    .sgpr_spill_count: 0
    .symbol:         _Z7gemm_dbILi256ELi192ELi64ELi96ELi64ELi2ELi1ELi4EEvPKDF16_S1_PfPDF16_S3_S3_PK15HIP_vector_typeIfLj2EEiii.kd
    .uniform_work_group_size: 1
    .uses_dynamic_stack: false
    .vgpr_count:     137
    .vgpr_spill_count: 0
    .wavefront_size: 64
  - .agpr_count:     0
    .args:
      - .address_space:  global
        .offset:         0
        .size:           8
        .value_kind:     global_buffer
      - .address_space:  global
        .offset:         8
        .size:           8
        .value_kind:     global_buffer
      - .address_space:  global
        .offset:         16
        .size:           8
        .value_kind:     global_buffer
      - .address_space:  global
        .offset:         24
        .size:           8
        .value_kind:     global_buffer
      - .address_space:  global
        .offset:         32
        .size:           8
        .value_kind:     global_buffer
      - .address_space:  global
        .offset:         40
        .size:           8
        .value_kind:     global_buffer
      - .actual_access:  read_only
        .address_space:  global
        .offset:         48
        .size:           8
        .value_kind:     global_buffer
      - .offset:         56
        .size:           4
        .value_kind:     by_value
      - .offset:         60
        .size:           4
        .value_kind:     by_value
      - .offset:         64
        .size:           4
        .value_kind:     by_value
    .group_segment_fixed_size: 0
    .kernarg_segment_align: 8
    .kernarg_segment_size: 68
    .language:       OpenCL C
    .language_version:
      - 2
      - 0
    .max_flat_workgroup_size: 512
    .name:           _Z7gemm_dbILi128ELi128ELi64ELi64ELi64ELi3ELi0ELi4EEvPKDF16_S1_PfPDF16_S3_S3_PK15HIP_vector_typeIfLj2EEiii
    .private_segment_fixed_size: 0
    .sgpr_count:     26
    .sgpr_spill_count: 0
    .symbol:         _Z7gemm_dbILi128ELi128ELi64ELi64ELi64ELi3ELi0ELi4EEvPKDF16_S1_PfPDF16_S3_S3_PK15HIP_vector_typeIfLj2EEiii.kd
    .uniform_work_group_size: 1
    .uses_dynamic_stack: false
    .vgpr_count:     168
    .vgpr_spill_count: 0
    .wavefront_size: 64
